# expert-weight conversion: the workgroups with two scan units / one more GEMM unit take the last ~6 percent of each conversion slot
# speedup vs baseline: 1.0069x; 1.0009x over previous
.LBB0_835:
	v_readlane_b32 s74, v254, 10
	v_readlane_b32 s75, v254, 11
	v_readlane_b32 s90, v254, 16
	s_load_dwordx4 s[84:87], s[74:75], 0xf8
	s_sub_i32 s0, 0x180, s90
	s_cmpk_lt_i32 s90, 0x180
	s_cselect_b32 s0, s0, 0
	v_readlane_b32 s88, v254, 18
	s_cmp_lt_i32 s88, s0
	v_readlane_b32 s83, v254, 14
	v_readlane_b32 s92, v254, 15
	s_waitcnt vmcnt(0) lgkmcnt(0)
	s_barrier
	v_readlane_b32 s91, v254, 17
	v_readlane_b32 s89, v254, 19
	s_cbranch_scc1 .Lmy_hw4
	s_mov_b32 s76, 13176
	s_mov_b32 s78, s88
	s_sub_i32 s11, s88, s0
	s_sub_i32 s1, s90, s0
	s_lshl_b32 s13, s11, 3
	s_mul_i32 s0, s83, 0x4200
	s_add_i32 s13, s13, s83
	s_lshl_b32 s10, s1, 3
	s_add_i32 s12, s0, 0
	s_cmpk_gt_u32 s13, 0x15ff
	s_cbranch_scc1 .LBB0_879
	v_and_b32_e32 v3, 7, v0
	v_lshlrev_b32_e32 v70, 2, v3
	v_lshlrev_b32_e32 v2, 4, v3
	v_mul_u32_u24_e32 v6, 0x840, v3
	v_mov_b32_e32 v3, 0
	s_add_u32 s0, s86, 0x940000
	v_add_u32_e32 v4, s12, v2
	v_lshl_add_u64 v[2:3], s[86:87], 0, v[2:3]
	s_mov_b64 s[2:3], 0x3b00000
	s_addc_u32 s1, s87, 0
	v_lshrrev_b32_e32 v71, 3, v162
	v_lshl_add_u64 v[66:67], v[2:3], 0, s[2:3]
	s_lshl_b32 s2, s90, 3
	s_max_i32 s3, s90, 0x180
	v_mul_u32_u24_e32 v5, 0x84, v71
	v_lshlrev_b32_e32 v2, 2, v71
	s_add_i32 s2, s83, s2
	s_lshl_b32 s3, s3, 3
	v_or_b32_e32 v72, 8, v71
	v_or_b32_e32 v73, 16, v71
	v_or_b32_e32 v74, 24, v71
	v_add3_u32 v75, s12, v6, v2
	s_sub_i32 s8, s2, s3
	s_lshl_b32 s9, s88, 3
	s_movk_i32 s14, 0xc8
	s_movk_i32 s15, 0x1600
	s_movk_i32 s16, 0x5800
	v_add_u32_e32 v76, v4, v5
	s_branch .LBB0_839

.LBB0_939:
	s_cmp_ge_i32 s13, s76
	s_cbranch_scc1 .LBB0_986
	s_add_u32 s3, s86, 0x29400000
	v_and_b32_e32 v2, 7, v0
	v_lshrrev_b32_e32 v73, 3, v162
	s_addc_u32 s13, s87, 0
	v_lshlrev_b32_e32 v72, 2, v2
	v_lshlrev_b32_e32 v66, 4, v2
	v_mul_u32_u24_e32 v2, 0x840, v2
	v_lshlrev_b32_e32 v5, 2, v73
	v_add_u32_e32 v3, s12, v66
	v_add3_u32 v77, s12, v2, v5
	s_add_u32 s12, s86, 0x13400000
	s_addc_u32 s14, s87, 0
	s_add_u32 s15, s86, 0x960000
	s_addc_u32 s16, s87, 0
	s_lshl_b32 s2, s90, 3
	s_max_i32 s4, s90, 0x180
	s_add_i32 s2, s83, s2
	s_lshl_b32 s5, s4, 3
	s_load_dwordx2 s[0:1], s[74:75], 0xf0
	s_sub_i32 s17, s2, s5
	s_lshl_b32 s2, s11, 8
	s_lshl_b32 s5, s83, 5
	s_add_i32 s19, s2, s5
	s_lshl_b32 s2, s90, 9
	s_lshl_b32 s5, s4, 8
	v_mul_u32_u24_e32 v4, 0x84, v73
	s_sub_i32 s20, s2, s5
	s_lshl_b32 s2, s11, 4
	s_lshl_b32 s5, s83, 1
	v_mov_b32_e32 v69, 0
	s_add_i32 s11, s2, s5
	s_lshl_b32 s2, s90, 5
	s_lshl_b32 s4, s4, 4
	v_add_u32_e32 v78, v3, v4
	v_or_b32_e32 v74, 8, v73
	v_or_b32_e32 v75, 16, v73
	v_or_b32_e32 v76, 24, v73
	v_mov_b32_e32 v67, v69
	s_lshl_b32 s18, s78, 3
	s_sub_i32 s21, s2, s4
	s_mov_b32 s2, 0x43800000
	v_add_u32_e32 v79, 0x420, v78
	v_add_u32_e32 v80, 0x428, v78
	v_add_u32_e32 v81, 0x840, v78
	v_add_u32_e32 v82, 0x848, v78
	v_add_u32_e32 v83, 0xc60, v78
	v_add_u32_e32 v84, 0xc68, v78
	v_add_u32_e32 v85, 0x1080, v78
	v_add_u32_e32 v86, 0x1088, v78
	v_add_u32_e32 v87, 0x14a0, v78
	v_add_u32_e32 v88, 0x14a8, v78
	v_add_u32_e32 v89, 0x18c0, v78
	v_add_u32_e32 v90, 0x18c8, v78
	v_add_u32_e32 v91, 0x1ce0, v78
	v_add_u32_e32 v92, 0x1ce8, v78
	v_add_u32_e32 v93, 0x2100, v78
	v_add_u32_e32 v94, 0x2108, v78
	v_add_u32_e32 v95, 0x2520, v78
	v_add_u32_e32 v96, 0x2528, v78
	v_add_u32_e32 v97, 0x2940, v78
	v_add_u32_e32 v98, 0x2948, v78
	v_add_u32_e32 v99, 0x2d60, v78
	v_add_u32_e32 v100, 0x2d68, v78
	v_add_u32_e32 v101, 0x3180, v78
	v_add_u32_e32 v102, 0x3188, v78
	v_add_u32_e32 v103, 0x35a0, v78
	v_add_u32_e32 v104, 0x35a8, v78
	v_add_u32_e32 v105, 0x39c0, v78
	v_add_u32_e32 v106, 0x39c8, v78
	v_add_u32_e32 v107, 0x3de0, v78
	v_add_u32_e32 v108, 0x3de8, v78
	s_mov_b32 s22, 0xc3e00000
	s_movk_i32 s23, 0x1600
	s_movk_i32 s24, 0xe8
	s_movk_i32 s25, 0x5800
	v_add_u32_e32 v109, 0x400, v77
	v_mov_b32_e32 v110, 0x43e00000
	v_add_u32_e32 v111, 0x600, v77
	s_branch .LBB0_943
.Lmy_hw4:
	s_cmp_eq_u32 s0, 0
	s_cbranch_scc1 .LBB0_986
	s_add_i32 s11, s88, 1647
	s_lshl_b32 s13, s11, 3
	s_add_i32 s13, s13, s83
	s_sub_i32 s1, s90, s0
	s_lshl_b32 s10, s1, 3
	s_mul_i32 s12, s83, 0x4200
	s_mov_b32 s76, 0x4200
	s_add_i32 s78, s88, 1775
	s_branch .LBB0_939

.LBB0_942:
	s_add_i32 s18, s18, s10
	s_add_i32 s4, s17, s18
	s_add_i32 s19, s19, s20
	s_add_i32 s11, s11, s21
	s_cmp_ge_i32 s4, s76
	s_cbranch_scc1 .LBB0_986

.LBB0_1248:
	s_abs_i32 s2, s90
	s_waitcnt vmcnt(0)
	v_cvt_f32_u32_e32 v2, s2
	s_sub_i32 s3, 0, s2
	v_rcp_iflag_f32_e32 v2, v2
	s_nop 0
	v_mul_f32_e32 v2, 0x4f7ffffe, v2
	v_cvt_u32_f32_e32 v2, v2
	s_nop 0
	v_readfirstlane_b32 s4, v2
	s_mul_i32 s3, s3, s4
	s_mul_hi_u32 s3, s4, s3
	s_add_i32 s4, s4, s3
	s_mul_hi_u32 s3, s4, 0x480
	s_mul_i32 s3, s3, s2
	s_sub_i32 s3, 0x480, s3
	s_sub_i32 s4, s3, s2
	s_cmp_ge_u32 s3, s2
	s_cselect_b32 s3, s4, s3
	s_sub_i32 s4, s3, s2
	s_cmp_ge_u32 s3, s2
	s_cselect_b32 s4, s4, s3
	s_cmp_eq_u32 s4, 0
	s_cselect_b64 s[2:3], -1, 0
	s_cmp_lt_i32 s88, s4
	s_cselect_b64 s[6:7], -1, 0
	s_or_b64 s[2:3], s[2:3], s[6:7]
	s_and_b64 vcc, exec, s[2:3]
	s_cbranch_vccnz .Lmy_hw6
	s_sub_i32 s2, s88, s4
	s_lshl_b32 s2, s2, 3
	s_add_i32 s2, s2, s83
	s_mov_b32 s76, 20951
.Lmy_join6:
	s_add_i32 s12, s2, 0x4200
	s_cmp_ge_i32 s12, s76
	s_cbranch_scc1 .LBB0_1296
	s_sub_i32 s3, s90, s4
	s_lshl_b32 s5, s3, 3
	s_mul_i32 s3, s83, 0x4200
	s_add_i32 s6, s3, 0
	s_add_i32 s12, s2, 0x4200
	s_add_u32 s13, s86, 0x29400000
	s_addc_u32 s14, s87, 0
	s_add_u32 s15, s86, 0x13400000
	s_load_dwordx2 s[2:3], s[74:75], 0xf0
	v_and_b32_e32 v2, 7, v0
	v_lshrrev_b32_e32 v73, 3, v162
	s_addc_u32 s16, s87, 0
	v_lshlrev_b32_e32 v72, 2, v2
	v_lshlrev_b32_e32 v66, 4, v2
	v_mul_u32_u24_e32 v2, 0x840, v2
	v_lshlrev_b32_e32 v5, 2, v73
	s_add_u32 s17, s86, 0x960000
	v_add_u32_e32 v3, s6, v66
	v_mul_u32_u24_e32 v4, 0x84, v73
	v_add3_u32 v77, s6, v2, v5
	s_addc_u32 s18, s87, 0
	s_lshl_b32 s6, s90, 8
	s_lshl_b32 s7, s4, 8
	v_mov_b32_e32 v69, 0
	s_sub_i32 s20, s6, s7
	s_lshl_b32 s6, s90, 4
	s_lshl_b32 s4, s4, 4
	v_add_u32_e32 v78, v3, v4
	v_or_b32_e32 v74, 8, v73
	v_or_b32_e32 v75, 16, v73
	v_or_b32_e32 v76, 24, v73
	v_mov_b32_e32 v67, v69
	s_lshl_b32 s19, s12, 5
	s_lshl_b32 s21, s12, 1
	s_sub_i32 s22, s6, s4
	s_mov_b32 s4, 0x43800000
	v_add_u32_e32 v79, 0x420, v78
	v_add_u32_e32 v80, 0x428, v78
	v_add_u32_e32 v81, 0x840, v78
	v_add_u32_e32 v82, 0x848, v78
	v_add_u32_e32 v83, 0xc60, v78
	v_add_u32_e32 v84, 0xc68, v78
	v_add_u32_e32 v85, 0x1080, v78
	v_add_u32_e32 v86, 0x1088, v78
	v_add_u32_e32 v87, 0x14a0, v78
	v_add_u32_e32 v88, 0x14a8, v78
	v_add_u32_e32 v89, 0x18c0, v78
	v_add_u32_e32 v90, 0x18c8, v78
	v_add_u32_e32 v91, 0x1ce0, v78
	v_add_u32_e32 v92, 0x1ce8, v78
	v_add_u32_e32 v93, 0x2100, v78
	v_add_u32_e32 v94, 0x2108, v78
	v_add_u32_e32 v95, 0x2520, v78
	v_add_u32_e32 v96, 0x2528, v78
	v_add_u32_e32 v97, 0x2940, v78
	v_add_u32_e32 v98, 0x2948, v78
	v_add_u32_e32 v99, 0x2d60, v78
	v_add_u32_e32 v100, 0x2d68, v78
	v_add_u32_e32 v101, 0x3180, v78
	v_add_u32_e32 v102, 0x3188, v78
	v_add_u32_e32 v103, 0x35a0, v78
	v_add_u32_e32 v104, 0x35a8, v78
	v_add_u32_e32 v105, 0x39c0, v78
	v_add_u32_e32 v106, 0x39c8, v78
	v_add_u32_e32 v107, 0x3de0, v78
	v_add_u32_e32 v108, 0x3de8, v78
	s_mov_b32 s23, 0xc3e00000
	s_movk_i32 s24, 0x1600
	s_movk_i32 s25, 0xe8
	s_movk_i32 s26, 0x5800
	v_add_u32_e32 v109, 0x400, v77
	v_mov_b32_e32 v110, 0x43e00000
	v_add_u32_e32 v111, 0x600, v77
	s_branch .LBB0_1253
.Lmy_hw6:
	s_cmp_eq_u32 s4, 0
	s_cbranch_scc1 .LBB0_1296
	s_lshl_b32 s2, s88, 3
	s_add_i32 s2, s2, s83
	s_add_i32 s2, s2, 4055
	s_mov_b32 s76, 0x61ae
	s_branch .Lmy_join6

.LBB0_1252:
	s_add_i32 s12, s12, s5
	s_add_i32 s19, s19, s20
	s_add_i32 s21, s21, s22
	s_cmp_lt_i32 s12, s76
	s_cbranch_scc0 .LBB0_1296

.LBB0_1544:
	s_abs_i32 s2, s90
	s_waitcnt vmcnt(0)
	v_cvt_f32_u32_e32 v2, s2
	s_sub_i32 s3, 0, s2
	v_rcp_iflag_f32_e32 v2, v2
	s_nop 0
	v_mul_f32_e32 v2, 0x4f7ffffe, v2
	v_cvt_u32_f32_e32 v2, v2
	s_nop 0
	v_readfirstlane_b32 s4, v2
	s_mul_i32 s3, s3, s4
	s_mul_hi_u32 s3, s4, s3
	s_add_i32 s4, s4, s3
	s_mul_hi_u32 s3, s4, 0x480
	s_mul_i32 s3, s3, s2
	s_sub_i32 s3, 0x480, s3
	s_sub_i32 s4, s3, s2
	s_cmp_ge_u32 s3, s2
	s_cselect_b32 s3, s4, s3
	s_sub_i32 s4, s3, s2
	s_cmp_ge_u32 s3, s2
	s_cselect_b32 s4, s4, s3
	s_cmp_eq_u32 s4, 0
	s_cselect_b64 s[2:3], -1, 0
	s_cmp_lt_i32 s88, s4
	s_cselect_b64 s[6:7], -1, 0
	s_or_b64 s[2:3], s[2:3], s[6:7]
	s_and_b64 vcc, exec, s[2:3]
	s_cbranch_vccnz .Lmy_hw10
	s_sub_i32 s2, s88, s4
	s_lshl_b32 s2, s2, 3
	s_add_i32 s2, s2, s83
	s_mov_b32 s76, 37915
.Lmy_join10:
	s_add_i32 s12, s2, 0x61ae
	s_cmp_ge_i32 s12, s76
	s_cbranch_scc1 .LBB0_1592
	s_sub_i32 s3, s90, s4
	s_lshl_b32 s5, s3, 3
	s_mul_i32 s3, s83, 0x4200
	s_add_i32 s6, s3, 0
	s_add_i32 s12, s2, 0x61ae
	s_add_u32 s13, s86, 0x29400000
	s_addc_u32 s14, s87, 0
	s_add_u32 s15, s86, 0x13400000
	s_load_dwordx2 s[2:3], s[74:75], 0xf0
	v_and_b32_e32 v2, 7, v0
	v_lshrrev_b32_e32 v73, 3, v162
	s_addc_u32 s16, s87, 0
	v_lshlrev_b32_e32 v72, 2, v2
	v_lshlrev_b32_e32 v66, 4, v2
	v_mul_u32_u24_e32 v2, 0x840, v2
	v_lshlrev_b32_e32 v5, 2, v73
	s_add_u32 s17, s86, 0x960000
	v_add_u32_e32 v3, s6, v66
	v_mul_u32_u24_e32 v4, 0x84, v73
	v_add3_u32 v77, s6, v2, v5
	s_addc_u32 s18, s87, 0
	s_lshl_b32 s6, s90, 8
	s_lshl_b32 s7, s4, 8
	v_mov_b32_e32 v69, 0
	s_sub_i32 s20, s6, s7
	s_lshl_b32 s6, s90, 4
	s_lshl_b32 s4, s4, 4
	v_add_u32_e32 v78, v3, v4
	v_or_b32_e32 v74, 8, v73
	v_or_b32_e32 v75, 16, v73
	v_or_b32_e32 v76, 24, v73
	v_mov_b32_e32 v67, v69
	s_lshl_b32 s19, s12, 5
	s_lshl_b32 s21, s12, 1
	s_sub_i32 s22, s6, s4
	s_mov_b32 s4, 0x43800000
	v_add_u32_e32 v79, 0x420, v78
	v_add_u32_e32 v80, 0x428, v78
	v_add_u32_e32 v81, 0x840, v78
	v_add_u32_e32 v82, 0x848, v78
	v_add_u32_e32 v83, 0xc60, v78
	v_add_u32_e32 v84, 0xc68, v78
	v_add_u32_e32 v85, 0x1080, v78
	v_add_u32_e32 v86, 0x1088, v78
	v_add_u32_e32 v87, 0x14a0, v78
	v_add_u32_e32 v88, 0x14a8, v78
	v_add_u32_e32 v89, 0x18c0, v78
	v_add_u32_e32 v90, 0x18c8, v78
	v_add_u32_e32 v91, 0x1ce0, v78
	v_add_u32_e32 v92, 0x1ce8, v78
	v_add_u32_e32 v93, 0x2100, v78
	v_add_u32_e32 v94, 0x2108, v78
	v_add_u32_e32 v95, 0x2520, v78
	v_add_u32_e32 v96, 0x2528, v78
	v_add_u32_e32 v97, 0x2940, v78
	v_add_u32_e32 v98, 0x2948, v78
	v_add_u32_e32 v99, 0x2d60, v78
	v_add_u32_e32 v100, 0x2d68, v78
	v_add_u32_e32 v101, 0x3180, v78
	v_add_u32_e32 v102, 0x3188, v78
	v_add_u32_e32 v103, 0x35a0, v78
	v_add_u32_e32 v104, 0x35a8, v78
	v_add_u32_e32 v105, 0x39c0, v78
	v_add_u32_e32 v106, 0x39c8, v78
	v_add_u32_e32 v107, 0x3de0, v78
	v_add_u32_e32 v108, 0x3de8, v78
	s_mov_b32 s23, 0xc3e00000
	s_movk_i32 s24, 0x1600
	s_movk_i32 s25, 0xe8
	s_movk_i32 s26, 0x5800
	v_add_u32_e32 v109, 0x400, v77
	v_mov_b32_e32 v110, 0x43e00000
	v_add_u32_e32 v111, 0x600, v77
	s_branch .LBB0_1549
.Lmy_hw10:
	s_cmp_eq_u32 s4, 0
	s_cbranch_scc1 .LBB0_1592
	s_lshl_b32 s2, s88, 3
	s_add_i32 s2, s2, s83
	s_add_i32 s2, s2, 12909
	s_mov_b32 s76, 0xa3ae
	s_branch .Lmy_join10

.LBB0_2043:
	v_readlane_b32 s74, v254, 10
	v_readlane_b32 s75, v254, 11
	v_readlane_b32 s90, v254, 16
	s_load_dwordx4 s[84:87], s[74:75], 0xf8
	s_sub_i32 s0, 0x180, s90
	s_cmpk_lt_i32 s90, 0x180
	s_cselect_b32 s0, s0, 0
	v_readlane_b32 s88, v254, 18
	s_cmp_lt_i32 s88, s0
	v_readlane_b32 s83, v254, 14
	v_readlane_b32 s92, v254, 15
	s_waitcnt vmcnt(0) lgkmcnt(0)
	s_barrier
	v_readlane_b32 s91, v254, 17
	v_readlane_b32 s89, v254, 19
	s_cbranch_scc1 .Lmy_hw14
	s_sub_i32 s1, s88, s0
	s_lshl_b32 s1, s1, 3
	s_add_i32 s1, s1, s83
	s_mov_b32 s76, 63326
	s_mov_b32 s77, 0xa3ae
.Lmy_join14:
	s_add_i32 s4, s1, 0xa3ae
	s_cmp_ge_i32 s4, s76
	s_cbranch_scc1 .LBB0_2091
	s_sub_i32 s0, s90, s0
	s_lshl_b32 s3, s0, 3
	s_mul_i32 s0, s83, 0x4200
	s_add_i32 s2, s0, 0
	s_add_i32 s4, s1, 0xa3ae
	s_add_u32 s10, s86, 0x29400000
	s_addc_u32 s11, s87, 0
	s_add_u32 s12, s86, 0x13400000
	v_and_b32_e32 v2, 7, v0
	v_lshrrev_b32_e32 v73, 3, v162
	s_addc_u32 s13, s87, 0
	v_lshlrev_b32_e32 v72, 2, v2
	v_lshlrev_b32_e32 v66, 4, v2
	v_mul_u32_u24_e32 v2, 0x840, v2
	v_lshlrev_b32_e32 v5, 2, v73
	s_add_u32 s14, s86, 0x960000
	v_add_u32_e32 v3, s2, v66
	v_add3_u32 v77, s2, v2, v5
	s_addc_u32 s15, s87, 0
	s_lshl_b32 s2, s90, 3
	s_lshl_b32 s5, s88, 3
	s_load_dwordx2 s[0:1], s[74:75], 0xf0
	s_add_i32 s2, s2, s5
	s_max_i32 s5, s90, 0x180
	s_lshl_b32 s6, s5, 3
	v_mul_u32_u24_e32 v4, 0x84, v73
	s_sub_i32 s16, s2, s6
	s_lshl_b32 s2, s90, 9
	s_lshl_b32 s6, s5, 8
	v_mov_b32_e32 v69, 0
	s_lshl_b32 s18, s4, 5
	s_sub_i32 s19, s2, s6
	s_lshl_b32 s20, s4, 1
	s_lshl_b32 s2, s90, 5
	s_lshl_b32 s4, s5, 4
	v_add_u32_e32 v78, v3, v4
	v_or_b32_e32 v74, 8, v73
	v_or_b32_e32 v75, 16, v73
	v_or_b32_e32 v76, 24, v73
	v_mov_b32_e32 v67, v69
	s_add_i32 s17, s83, s77
	s_sub_i32 s21, s2, s4
	s_mov_b32 s2, 0x43800000
	v_add_u32_e32 v79, 0x420, v78
	v_add_u32_e32 v80, 0x428, v78
	v_add_u32_e32 v81, 0x840, v78
	v_add_u32_e32 v82, 0x848, v78
	v_add_u32_e32 v83, 0xc60, v78
	v_add_u32_e32 v84, 0xc68, v78
	v_add_u32_e32 v85, 0x1080, v78
	v_add_u32_e32 v86, 0x1088, v78
	v_add_u32_e32 v87, 0x14a0, v78
	v_add_u32_e32 v88, 0x14a8, v78
	v_add_u32_e32 v89, 0x18c0, v78
	v_add_u32_e32 v90, 0x18c8, v78
	v_add_u32_e32 v91, 0x1ce0, v78
	v_add_u32_e32 v92, 0x1ce8, v78
	v_add_u32_e32 v93, 0x2100, v78
	v_add_u32_e32 v94, 0x2108, v78
	v_add_u32_e32 v95, 0x2520, v78
	v_add_u32_e32 v96, 0x2528, v78
	v_add_u32_e32 v97, 0x2940, v78
	v_add_u32_e32 v98, 0x2948, v78
	v_add_u32_e32 v99, 0x2d60, v78
	v_add_u32_e32 v100, 0x2d68, v78
	v_add_u32_e32 v101, 0x3180, v78
	v_add_u32_e32 v102, 0x3188, v78
	v_add_u32_e32 v103, 0x35a0, v78
	v_add_u32_e32 v104, 0x35a8, v78
	v_add_u32_e32 v105, 0x39c0, v78
	v_add_u32_e32 v106, 0x39c8, v78
	v_add_u32_e32 v107, 0x3de0, v78
	v_add_u32_e32 v108, 0x3de8, v78
	s_mov_b32 s22, 0xc3e00000
	s_movk_i32 s23, 0x1600
	s_movk_i32 s24, 0xe8
	s_movk_i32 s25, 0x5800
	v_add_u32_e32 v109, 0x400, v77
	v_mov_b32_e32 v110, 0x43e00000
	v_add_u32_e32 v111, 0x600, v77
	s_branch .LBB0_2048
.Lmy_hw14:
	s_cmp_eq_u32 s0, 0
	s_cbranch_scc1 .LBB0_2091
	s_lshl_b32 s1, s88, 3
	s_add_i32 s1, s1, s83
	s_add_i32 s1, s1, 21424
	s_mov_b32 s76, 0x10800
	s_mov_b32 s77, 64350
	s_branch .Lmy_join14

.LBB0_2047:
	s_add_i32 s17, s17, s3
	s_add_i32 s4, s16, s17
	s_add_i32 s18, s18, s19
	s_add_i32 s20, s20, s21
	s_cmp_lt_i32 s4, s76
	s_cbranch_scc0 .LBB0_2091
